# static s_setprio 1 for the older half (waves 0-3) across the P4 mLSTM phase, reset at phase end
# speedup vs baseline: 1.0055x; 1.0055x over previous
.LBB0_609:
	s_or_b64 exec, exec, s[0:1]
	v_mov_b32_e32 v108, v0
	s_waitcnt lgkmcnt(0)
	v_mov_b32_e32 v1, s76
	v_mov_b32_e32 v2, s77
	s_barrier
	s_add_i32 s0, 0, 0x25d38
	v_readfirstlane_b32 s1, v2
	v_mov_b32_e32 v2, s78
	v_mov_b32_e32 v4, s74
	v_mov_b32_e32 v5, s75
	v_mov_b32_e32 v2, s0
	ds_read_b64 v[2:3], v2
	v_readfirstlane_b32 s46, v4
	v_readfirstlane_b32 s2, v1
	v_readfirstlane_b32 s39, v5
	s_mov_b32 s35, 0
	s_waitcnt lgkmcnt(0)
	v_readfirstlane_b32 s4, v2
	v_readfirstlane_b32 s5, v3
	s_cmpk_gt_i32 s46, 0xff
	v_writelane_b32 v243, s4, 14
	v_readfirstlane_b32 s3, v108
	s_nop 0
	v_writelane_b32 v243, s5, 15
	s_cbranch_scc1 .LBB0_825
	v_readfirstlane_b32 s98, v0
	s_nop 3
	s_cmp_gt_u32 s98, 255
	s_cbranch_scc1 .Lp4oldprio0
	s_setprio 1
.Lp4oldprio0:
	s_add_u32 s4, s2, 0x7400000
	s_addc_u32 s5, s1, 0
	s_add_u32 s40, s2, 0x17e00000
	s_addc_u32 s41, s1, 0
	s_add_u32 s0, s2, 0x300000
	v_writelane_b32 v243, s0, 16
	s_addc_u32 s0, s1, 0
	v_writelane_b32 v243, s0, 17
	s_add_u32 s0, s2, 0x1a200000
	v_writelane_b32 v243, s0, 19
	s_addc_u32 s0, s1, 0
	s_ashr_i32 s28, s3, 6
	v_writelane_b32 v243, s0, 20
	s_mul_i32 s0, s28, 0x2080
	s_add_i32 s0, s0, 0
	s_add_i32 s47, s0, 0x14f00
	s_lshl_b32 s0, s46, 3
	s_add_i32 s42, s28, s0
	s_lshl_b32 s33, s39, 3
	s_cmpk_eq_i32 s39, 0x100
	s_cselect_b64 s[8:9], -1, 0
	s_and_b64 s[6:7], s[8:9], exec
	s_movk_i32 s0, 0x330
	v_cmp_gt_i32_e64 s[6:7], s0, v108
	v_and_b32_e32 v1, 3, v108
	s_cselect_b32 s16, 0x4800, 0
	v_writelane_b32 v243, s6, 21
	s_cselect_b32 s18, 0xffffb800, 0
	s_lshl_b32 s17, s28, 4
	v_writelane_b32 v243, s7, 22
	v_cmp_eq_u32_e64 s[6:7], 0, v1
	v_ashrrev_i32_e32 v123, 2, v108
	s_movk_i32 s0, 0x70
	v_writelane_b32 v243, s6, 23
	s_cmp_gt_u32 s3, 63
	v_and_b32_e32 v111, 63, v108
	v_writelane_b32 v243, s7, 24
	s_movk_i32 s6, 0x8ff
	v_cmp_lt_i32_e64 s[6:7], s6, v108
	v_mul_lo_u32 v2, v123, s0
	v_add_u32_e32 v110, 0, v2
	v_writelane_b32 v243, s6, 25
	v_lshlrev_b32_e32 v2, 1, v111
	v_lshlrev_b32_e32 v112, 3, v1
	v_writelane_b32 v243, s7, 26
	s_cselect_b64 s[6:7], -1, 0
	s_cmp_lt_u32 s3, 64
	s_cselect_b64 s[10:11], -1, 0
	s_add_i32 s29, 0, 0x10700
	s_movk_i32 s3, 0xa0
	v_sub_u32_e32 v156, 0, v2
	v_mad_u64_u32 v[2:3], s[14:15], v123, s3, v[110:111]
	v_lshlrev_b32_e32 v118, 4, v1
	s_add_u32 s43, s2, 0x2ce00000
	v_and_b32_e32 v1, 7, v108
	v_bfe_u32 v158, v108, 3, 3
	s_addc_u32 s44, s1, 0
	v_mul_u32_u24_e32 v3, 0x410, v1
	v_lshlrev_b32_e32 v7, 2, v158
	s_add_i32 s1, 0, 0x8800
	v_add3_u32 v159, s47, v3, v7
	v_add_u32_e32 v3, s1, v112
	s_lshl_b32 s2, s28, 5
	s_mul_i32 s1, s39, 0x88
	s_add_i32 s2, s2, 0
	s_add_i32 s19, s42, s1
	v_bfe_u32 v113, v108, 4, 2
	s_cmp_lt_i32 s19, s16
	v_and_b32_e32 v117, 15, v108
	v_lshlrev_b32_e32 v122, 2, v113
	s_cselect_b64 s[14:15], -1, 0
	v_or_b32_e32 v151, s17, v117
	v_sub_u32_e32 v244, v151, v122
	v_subrev_u32_e32 v245, 64, v244
	v_or_b32_e32 v7, s17, v122
	s_and_b64 s[16:17], s[14:15], exec
	s_cselect_b32 s1, 0, s18
	s_add_i32 s3, s1, s19
	s_mul_hi_i32 s1, s3, 0x30c30c31
	s_and_b64 s[20:21], s[8:9], s[14:15]
	s_lshr_b32 s14, s1, 31
	s_ashr_i32 s1, s1, 10
	s_add_i32 s1, s1, s14
	v_writelane_b32 v243, s10, 27
	s_mul_i32 s14, s1, 0xffffeb00
	s_add_i32 s31, s14, s3
	v_writelane_b32 v243, s11, 28
	s_and_b64 s[14:15], s[20:21], exec
	v_writelane_b32 v243, s20, 29
	v_cmp_gt_i32_e64 s[50:51], v122, v151
	v_lshl_add_u32 v11, v7, 1, 0
	v_writelane_b32 v243, s21, 30
	v_writelane_b32 v243, s50, 31
	v_or_b32_e32 v7, 2, v122
	s_brev_b32 s3, 16
	v_writelane_b32 v243, s51, 32
	v_cmp_lt_i32_e64 s[50:51], v122, v151
	s_cselect_b32 s3, s3, 0xc600000
	s_lshl_b32 s14, s31, 1
	v_writelane_b32 v243, s50, 33
	s_add_i32 s14, s14, 0x7fffe400
	s_and_b32 s30, s14, 0x7fffffc0
	v_writelane_b32 v243, s51, 34
	v_cmp_gt_i32_e64 s[50:51], v7, v151
	v_or_b32_e32 v7, 3, v122
	s_lshl_b32 s14, s19, 5
	v_writelane_b32 v243, s50, 35
	s_and_b32 s34, s14, 0x3e0
	s_and_b64 s[14:15], s[20:21], exec
	v_writelane_b32 v243, s51, 36
	v_cmp_gt_i32_e64 s[50:51], v7, v151
	v_or_b32_e32 v7, 16, v122
	s_mov_b32 s16, 0x1000000
	v_writelane_b32 v243, s50, 37
	s_mul_hi_i32 s14, s31, 0x92492493
	s_cselect_b32 s36, s16, 0xb800000
	v_writelane_b32 v243, s51, 38
	v_cmp_gt_i32_e64 s[50:51], v7, v151
	v_or_b32_e32 v7, 17, v122
	s_add_i32 s14, s14, s31
	v_writelane_b32 v243, s50, 39
	s_lshr_b32 s15, s14, 31
	s_ashr_i32 s14, s14, 7
	v_writelane_b32 v243, s51, 40
	v_cmp_gt_i32_e64 s[50:51], v7, v151
	v_or_b32_e32 v7, 18, v122
	s_add_i32 s14, s14, s15
	v_writelane_b32 v243, s50, 41
	s_lshl_b32 s37, s14, 6
	s_mulk_i32 s14, 0xe0
	v_writelane_b32 v243, s51, 42
	v_cmp_gt_i32_e64 s[50:51], v7, v151
	v_or_b32_e32 v7, 19, v122
	s_sub_i32 s14, s31, s14
	v_writelane_b32 v243, s50, 43
	s_lshl_b32 s38, s14, 5
	s_cmp_gt_i32 s28, -1
	v_writelane_b32 v243, s51, 44
	v_cmp_gt_i32_e64 s[50:51], v7, v151
	v_or_b32_e32 v7, 32, v122
	s_cselect_b64 s[84:85], -1, 0
	v_writelane_b32 v243, s50, 45
	s_cmp_gt_i32 s28, 0
	s_cselect_b64 s[14:15], -1, 0
	v_writelane_b32 v243, s51, 46
	v_cmp_gt_i32_e64 s[50:51], v7, v151
	v_or_b32_e32 v7, 33, v122
	s_cmp_gt_i32 s28, 1
	v_writelane_b32 v243, s50, 47
	s_cselect_b64 s[16:17], -1, 0
	s_cmp_gt_i32 s28, 2
	v_writelane_b32 v243, s51, 48
	v_cmp_gt_i32_e64 s[50:51], v7, v151
	v_or_b32_e32 v7, 34, v122
	s_cselect_b64 s[18:19], -1, 0
	v_writelane_b32 v243, s50, 49
	s_cmp_gt_i32 s28, 3
	s_cselect_b64 s[20:21], -1, 0
	v_writelane_b32 v243, s51, 50
	v_cmp_gt_i32_e64 s[50:51], v7, v151
	v_or_b32_e32 v7, 35, v122
	s_cmp_gt_i32 s28, 4
	v_writelane_b32 v243, s50, 51
	s_cselect_b64 s[22:23], -1, 0
	s_cmp_gt_i32 s28, 5
	v_writelane_b32 v243, s51, 52
	v_cmp_gt_i32_e64 s[50:51], v7, v151
	v_or_b32_e32 v7, 48, v122
	v_bfe_u32 v5, v108, 2, 2
	v_writelane_b32 v243, s50, 53
	v_lshlrev_b32_e32 v116, 3, v113
	v_lshlrev_b32_e32 v6, 2, v111
	v_writelane_b32 v243, s51, 54
	v_cmp_gt_i32_e64 s[50:51], v7, v151
	v_or_b32_e32 v7, 49, v122
	s_cselect_b64 s[24:25], -1, 0
	v_writelane_b32 v243, s50, 55
	s_cmp_gt_i32 s28, 6
	v_add_u32_e32 v153, s29, v6
	v_writelane_b32 v243, s51, 56
	v_cmp_gt_i32_e64 s[50:51], v7, v151
	v_or_b32_e32 v7, 50, v122
	v_add_u32_e32 v155, 0, v6
	v_writelane_b32 v243, s50, 57
	v_and_b32_e32 v163, 28, v6
	v_or_b32_e32 v6, v116, v5
	v_writelane_b32 v243, s51, 58
	v_cmp_gt_i32_e64 s[50:51], v7, v151
	v_or_b32_e32 v7, 51, v122
	s_cselect_b64 s[26:27], -1, 0
	v_writelane_b32 v243, s50, 59
	s_cmpk_lt_i32 s31, 0xe00
	v_or_b32_e32 v5, v122, v5
	v_writelane_b32 v243, s51, 60
	v_cmp_gt_i32_e64 s[50:51], v7, v151
	v_or_b32_e32 v7, 64, v122
	v_mad_u32_u24 v164, v5, s0, v3
	v_writelane_b32 v243, s50, 61
	v_mul_u32_u24_e32 v5, 0x110, v6
	v_mad_u32_u24 v169, v6, s0, v3
	v_writelane_b32 v243, s51, 62
	v_cmp_gt_i32_e64 s[50:51], v7, v151
	v_or_b32_e32 v7, 0x41, v122
	s_movk_i32 s0, 0x400
	v_writelane_b32 v243, s50, 63
	s_cselect_b32 s3, s36, s3
	s_mov_b32 s31, 0xe00000
	v_writelane_b32 v242, s51, 0
	v_cmp_gt_i32_e64 s[50:51], v7, v151
	v_or_b32_e32 v7, 0x42, v122
	v_add3_u32 v168, s2, v112, v5
	v_writelane_b32 v242, s50, 1
	s_cselect_b32 s2, s0, 0xe00
	s_cselect_b32 s0, s37, s30
	v_writelane_b32 v242, s51, 2
	v_cmp_gt_i32_e64 s[50:51], v7, v151
	v_or_b32_e32 v7, 0x43, v122
	s_cselect_b32 s30, s38, s34
	v_writelane_b32 v242, s50, 3
	s_cselect_b32 s31, s31, 0x700000
	s_add_u32 s3, s43, s3
	v_writelane_b32 v242, s51, 4
	v_cmp_gt_i32_e64 s[50:51], v7, v151
	v_or_b32_e32 v7, 0x50, v122
	v_cmp_gt_i32_e64 s[56:57], v7, v151
	v_or_b32_e32 v7, 0x51, v122
	v_cmp_gt_i32_e64 s[58:59], v7, v151
	v_or_b32_e32 v7, 0x52, v122
	v_cmp_gt_i32_e64 s[60:61], v7, v151
	v_or_b32_e32 v7, 0x53, v122
	v_cmp_gt_i32_e64 s[62:63], v7, v151
	v_or_b32_e32 v7, 0x60, v122
	v_cmp_gt_i32_e64 s[64:65], v7, v151
	v_or_b32_e32 v7, 0x61, v122
	v_cmp_gt_i32_e64 s[66:67], v7, v151
	v_or_b32_e32 v7, 0x62, v122
	s_addc_u32 s34, s44, 0
	s_mul_hi_i32 s36, s31, s1
	s_mul_i32 s31, s31, s1
	v_cmp_gt_i32_e64 s[68:69], v7, v151
	v_or_b32_e32 v7, 0x63, v122
	s_add_u32 s3, s3, s31
	v_cmp_gt_i32_e64 s[70:71], v7, v151
	v_or_b32_e32 v7, 0x70, v122
	s_addc_u32 s31, s34, s36
	s_ashr_i32 s1, s0, 31
	v_cmp_gt_i32_e64 s[72:73], v7, v151
	v_or_b32_e32 v7, 0x71, v122
	s_lshl_b64 s[0:1], s[0:1], 1
	v_mov_b32_e32 v115, 0
	v_and_b32_e32 v114, 48, v108
	v_cmp_gt_i32_e64 s[74:75], v7, v151
	v_or_b32_e32 v7, 0x72, v122
	s_add_u32 s0, s3, s0
	v_lshlrev_b32_e32 v4, 3, v1
	v_or_b32_e32 v160, 8, v158
	v_lshl_add_u64 v[120:121], s[40:41], 0, v[114:115]
	v_add_u32_e32 v10, 0, v114
	v_cmp_gt_i32_e64 s[76:77], v7, v151
	v_or_b32_e32 v7, 0x73, v122
	s_addc_u32 s1, s31, s1
	v_lshlrev_b32_e32 v114, 4, v1
	v_or_b32_e32 v1, s30, v158
	v_or_b32_e32 v161, 16, v158
	v_cmp_gt_i32_e64 s[78:79], v7, v151
	v_lshl_add_u64 v[6:7], s[0:1], 0, v[114:115]
	v_mad_i64_i32 v[8:9], s[0:1], s2, v1, 0
	v_or_b32_e32 v1, s30, v160
	v_or_b32_e32 v162, 24, v158
	v_lshl_add_u64 v[124:125], v[8:9], 1, v[6:7]
	v_mad_i64_i32 v[8:9], s[0:1], s2, v1, 0
	v_or_b32_e32 v1, s30, v161
	v_writelane_b32 v242, s50, 5
	v_lshl_add_u64 v[126:127], v[8:9], 1, v[6:7]
	v_mad_i64_i32 v[8:9], s[0:1], s2, v1, 0
	v_or_b32_e32 v1, s30, v162
	v_writelane_b32 v242, s51, 6
	v_lshl_add_u64 v[128:129], v[8:9], 1, v[6:7]
	v_mad_i64_i32 v[8:9], s[0:1], s2, v1, 0
	v_max_i32_e32 v1, 0x700, v108
	v_writelane_b32 v242, s43, 7
	v_sub_u32_e32 v1, v1, v108
	v_writelane_b32 v242, s44, 9
	s_lshl_b32 s0, s42, 5
	v_add_u32_e32 v1, 0x1ff, v1
	v_lshlrev_b32_e32 v176, 2, v108
	v_lshl_add_u64 v[130:131], v[8:9], 1, v[6:7]
	v_writelane_b32 v242, s42, 10
	s_and_b32 s0, s0, 0x3e0
	v_add_u32_e32 v3, 0, v176
	v_lshlrev_b32_e32 v8, 2, v1
	v_writelane_b32 v242, s0, 11
	v_add_u32_e32 v3, 0x12b00, v3
	s_movk_i32 s0, 0xdff
	v_and_b32_e32 v8, 0xfffff800, v8
	v_lshrrev_b32_e32 v5, 9, v1
	v_cmp_lt_u32_e32 vcc, s0, v1
	v_cmp_gt_u32_e64 s[0:1], 2.0, v1
	v_add_u32_e32 v1, v3, v8
	v_add_u32_e32 v6, 1, v5
	v_add_u32_e32 v5, -1, v5
	v_cmp_ge_u32_e64 s[2:3], v1, v3
	s_and_b64 s[0:1], s[2:3], s[0:1]
	v_cmp_lt_u32_e64 s[2:3], 1, v5
	v_lshrrev_b32_e32 v7, 1, v5
	v_and_b32_e32 v5, 2, v5
	v_writelane_b32 v242, s2, 13
	v_and_b32_e32 v3, 0xfffffe, v6
	s_and_b64 s[0:1], vcc, s[0:1]
	v_writelane_b32 v242, s3, 14
	v_cmp_eq_u32_e64 s[2:3], 0, v5
	v_mov_b32_e32 v119, v115
	v_and_b32_e32 v12, 0x7f, v108
	v_writelane_b32 v242, s2, 15
	v_lshl_add_u32 v177, v3, 9, v108
	v_mul_u32_u24_e32 v13, 0x110, v117
	v_writelane_b32 v242, s3, 16
	v_cmp_ne_u32_e64 s[2:3], v6, v3
	v_lshl_add_u32 v3, v108, 4, 0
	v_or_b32_e32 v132, 0xffffff00, v12
	v_writelane_b32 v242, s2, 17
	v_add_u32_e32 v7, 1, v7
	v_add_u32_e32 v179, 0xc000, v3
	v_writelane_b32 v242, s3, 18
	v_writelane_b32 v242, s0, 19
	v_mbcnt_hi_u32_b32 v184, -1, v212
	v_bfrev_b32_e32 v6, 0.5
	v_writelane_b32 v242, s1, 20
	v_writelane_b32 v242, s40, 21
	s_lshl_b32 s1, s28, 1
	s_movk_i32 s49, 0x100
	v_writelane_b32 v242, s41, 22
	v_lshl_add_u64 v[134:135], s[40:41], 0, v[118:119]
	s_lshl_b32 s41, s39, 4
	v_writelane_b32 v242, s39, 23
	s_sub_i32 s0, 0, s41
	v_writelane_b32 v242, s0, 24
	s_lshl_b32 s0, s46, 4
	s_add_i32 s0, s0, s1
	s_add_i32 s0, s0, 0x7fffe400
	v_writelane_b32 v242, s0, 25
	s_add_i32 s0, 0, 0x25de0
	v_writelane_b32 v242, s0, 27
	s_add_i32 s0, 0, 0x25dd0
	v_writelane_b32 v242, s0, 29
	s_add_i32 s0, s47, 0x820
	v_writelane_b32 v242, s0, 30
	s_add_i32 s0, s47, 0xc30
	v_writelane_b32 v242, s0, 31
	s_add_i32 s0, s47, 0x1040
	v_writelane_b32 v242, s0, 33
	s_add_i32 s0, s47, 0x1450
	v_writelane_b32 v242, s0, 34
	s_add_i32 s0, s47, 0x1860
	v_writelane_b32 v242, s0, 35
	v_sub_u32_e32 v133, 0xff, v123
	v_sub_u32_e32 v152, 0xff, v151
	v_add_u32_e32 v154, 0x100, v153
	v_cmp_lt_u32_e64 s[10:11], 15, v111
	v_cmp_eq_u32_e64 s[12:13], 0, v111
	v_add_u32_e32 v157, 0xffffff00, v151
	v_add_u32_e32 v165, 0xe00, v164
	v_add_u32_e32 v166, 0x1c00, v164
	v_add_u32_e32 v167, 0x2a00, v164
	v_add_u32_e32 v170, 0x2200, v168
	v_add_u32_e32 v171, 0xe00, v169
	v_add_u32_e32 v172, 0x4400, v168
	v_add_u32_e32 v173, 0x1c00, v169
	v_add_u32_e32 v174, 0x6600, v168
	v_add_u32_e32 v175, 0x2a00, v169
	v_mov_b32_e32 v1, v132
	v_add_u32_e32 v109, 0x200, v108
	v_and_b32_e32 v178, -2, v7
	v_add_u32_e32 v119, 0xfffffe00, v108
	v_add_u32_e32 v180, s29, v176
	s_sub_i32 s40, 0, s33
	v_add_u32_e32 v181, 0x10900, v155
	v_sub_u32_e32 v182, 0, v123
	v_lshlrev_b32_e32 v136, 1, v116
	s_mov_b32 s42, 0x3f2aaaab
	v_mov_b32_e32 v183, 0x3ecc95a3
	s_mov_b32 s43, 0x3f317218
	s_mov_b32 s44, 0x7f800000
	s_mov_b32 s45, 0x33800000
	v_lshlrev_b32_e32 v138, 2, v122
	v_add_u32_e32 v185, v2, v118
	s_xor_b64 s[28:29], s[8:9], -1
	v_lshlrev_b32_e32 v114, 1, v4
	v_writelane_b32 v242, s47, 36
	s_add_i32 s0, s47, 0x1c70
	v_add_u32_e32 v186, v11, v13
	v_mov_b32_e32 v2, v115
	v_mov_b32_e32 v3, v115
	v_mov_b32_e32 v4, v115
	v_mov_b32_e32 v5, v115
	v_mov_b32_e32 v140, 0x3f317218
	v_mov_b32_e32 v187, 0x7f800000
	v_mov_b32_e32 v188, 0x7fc00000
	v_mov_b32_e32 v189, 0xff800000
	v_lshl_or_b32 v190, v184, 2, v6
	v_add_u32_e32 v191, v10, v13
	v_mov_b32_e32 v192, 0x7c
	v_writelane_b32 v242, s0, 38
	s_branch .LBB0_612

.LBB0_2009:
	s_add_i32 s3, 0, 0x25d38
	v_mov_b32_e32 v1, s3
	ds_read_b64 v[2:3], v1
	v_readfirstlane_b32 s3, v104
	s_cmpk_gt_i32 s54, 0xff
	s_waitcnt lgkmcnt(0)
	v_readfirstlane_b32 s4, v2
	v_readfirstlane_b32 s5, v3
	s_nop 0
	v_writelane_b32 v243, s4, 25
	s_nop 1
	v_writelane_b32 v243, s5, 26
	s_cbranch_scc1 .LBB0_2237
	v_readfirstlane_b32 s98, v0
	s_nop 3
	s_cmp_gt_u32 s98, 255
	s_cbranch_scc1 .Lp4oldprio1
	s_setprio 1
.Lp4oldprio1:
	s_or_b32 s42, s0, s33
	s_add_u32 s4, s2, 0x7400000
	s_addc_u32 s5, s1, 0
	s_add_u32 s36, s2, 0x17e00000
	s_addc_u32 s37, s1, 0
	s_add_u32 s0, s2, 0x300000
	v_writelane_b32 v242, s0, 41
	s_addc_u32 s0, s1, 0
	v_writelane_b32 v242, s0, 43
	s_add_u32 s0, s2, 0x1a200000
	v_writelane_b32 v243, s0, 29
	s_addc_u32 s0, s1, 0
	s_ashr_i32 s26, s3, 6
	v_writelane_b32 v242, s0, 25
	s_mul_i32 s0, s26, 0x2080
	s_add_i32 s43, s0, 0
	s_lshl_b32 s0, s54, 3
	s_add_i32 s15, s26, s0
	s_movk_i32 s0, 0x330
	v_cmp_gt_i32_e64 s[6:7], s0, v104
	v_readlane_b32 s14, v243, 23
	v_and_b32_e32 v1, 3, v104
	v_writelane_b32 v243, s6, 17
	s_add_i32 s43, s43, 0x14f00
	s_lshl_b32 s44, s14, 3
	v_writelane_b32 v243, s7, 18
	v_cmp_eq_u32_e64 s[6:7], 0, v1
	s_lshl_b32 s9, s26, 4
	s_cmp_gt_u32 s3, 63
	v_writelane_b32 v242, s6, 19
	v_and_b32_e32 v107, 63, v104
	v_ashrrev_i32_e32 v119, 2, v104
	v_writelane_b32 v242, s7, 20
	s_movk_i32 s6, 0x8ff
	v_cmp_lt_i32_e64 s[6:7], s6, v104
	s_movk_i32 s0, 0x70
	v_mul_lo_u32 v2, v119, s0
	v_writelane_b32 v242, s6, 13
	v_cmp_eq_u32_e64 s[12:13], 0, v107
	v_add_u32_e32 v106, 0, v2
	v_writelane_b32 v242, s7, 14
	s_cselect_b64 s[6:7], -1, 0
	s_cmp_lt_u32 s3, 64
	s_cselect_b64 s[10:11], -1, 0
	s_add_i32 s8, 0, 0x10700
	s_cmp_lg_u32 s42, 0
	v_lshlrev_b32_e32 v2, 1, v107
	v_writelane_b32 v243, s12, 31
	s_movk_i32 s3, 0xa0
	s_cselect_b64 s[84:85], -1, 0
	s_sub_i32 s45, 0, s33
	v_lshlrev_b32_e32 v108, 3, v1
	v_sub_u32_e32 v152, 0, v2
	v_writelane_b32 v243, s13, 32
	v_mad_u64_u32 v[2:3], s[12:13], v119, s3, v[106:107]
	v_lshlrev_b32_e32 v114, 4, v1
	s_add_u32 s38, s2, 0x2ce00000
	v_and_b32_e32 v1, 7, v104
	v_bfe_u32 v154, v104, 3, 3
	s_addc_u32 s39, s1, 0
	v_mul_u32_u24_e32 v3, 0x410, v1
	v_lshlrev_b32_e32 v7, 2, v154
	s_add_i32 s1, 0, 0x8800
	v_add3_u32 v155, s43, v3, v7
	v_add_u32_e32 v3, s1, v108
	s_lshl_b32 s2, s26, 5
	s_mul_i32 s1, s14, 0x88
	s_add_i32 s2, s2, 0
	s_add_i32 s1, s15, s1
	s_cmp_lt_i32 s1, s42
	s_cselect_b64 s[12:13], -1, 0
	s_cmp_ge_i32 s1, s33
	v_writelane_b32 v243, s15, 16
	s_cselect_b64 s[14:15], -1, 0
	s_and_b64 s[16:17], s[14:15], exec
	s_cselect_b32 s3, s45, s33
	s_add_i32 s18, s3, s1
	v_writelane_b32 v242, s10, 15
	s_mul_hi_i32 s1, s18, 0x30c30c31
	s_lshr_b32 s3, s1, 31
	v_writelane_b32 v242, s11, 16
	s_ashr_i32 s1, s1, 10
	v_readlane_b32 s16, v242, 27
	s_add_i32 s1, s1, s3
	v_readlane_b32 s17, v242, 28
	s_mul_i32 s3, s1, 0xffffeb00
	v_bfe_u32 v109, v104, 4, 2
	s_or_b64 s[14:15], s[16:17], s[14:15]
	s_add_i32 s35, s3, s18
	v_and_b32_e32 v113, 15, v104
	v_lshlrev_b32_e32 v118, 2, v109
	s_mov_b32 s3, 0xc600000
	s_and_b64 s[16:17], s[14:15], exec
	v_or_b32_e32 v147, s9, v113
	v_sub_u32_e32 v244, v147, v118
	v_subrev_u32_e32 v245, 64, v244
	v_or_b32_e32 v7, s9, v118
	s_cselect_b32 s3, s3, 0x8000000
	s_lshl_b32 s9, s35, 1
	s_add_i32 s9, s9, 0x7fffe400
	s_lshl_b32 s16, s18, 5
	s_and_b32 s9, s9, 0x7fffffc0
	s_and_b32 s28, s16, 0x3e0
	s_and_b64 s[14:15], s[14:15], exec
	s_mov_b32 s16, 0xb800000
	s_mul_hi_i32 s14, s35, 0x92492493
	s_cselect_b32 s29, s16, 0x1000000
	s_add_i32 s14, s14, s35
	s_lshr_b32 s15, s14, 31
	s_ashr_i32 s14, s14, 7
	s_add_i32 s14, s14, s15
	s_lshl_b32 s30, s14, 6
	s_mulk_i32 s14, 0xe0
	s_sub_i32 s14, s35, s14
	s_lshl_b32 s34, s14, 5
	s_cmp_gt_i32 s26, -1
	s_cselect_b64 s[82:83], -1, 0
	s_cmp_gt_i32 s26, 0
	s_cselect_b64 s[14:15], -1, 0
	s_cmp_gt_i32 s26, 1
	s_cselect_b64 s[16:17], -1, 0
	s_cmp_gt_i32 s26, 2
	s_cselect_b64 s[18:19], -1, 0
	s_cmp_gt_i32 s26, 3
	s_cselect_b64 s[20:21], -1, 0
	s_cmp_gt_i32 s26, 4
	s_cselect_b64 s[22:23], -1, 0
	s_cmp_gt_i32 s26, 5
	s_cselect_b64 s[24:25], -1, 0
	s_cmp_gt_i32 s26, 6
	s_cselect_b64 s[26:27], -1, 0
	s_and_b64 s[12:13], s[84:85], s[12:13]
	v_writelane_b32 v242, s12, 17
	v_lshl_add_u32 v11, v7, 1, 0
	v_or_b32_e32 v7, 2, v118
	v_writelane_b32 v242, s13, 18
	v_cmp_gt_i32_e64 s[12:13], v118, v147
	v_bfe_u32 v5, v104, 2, 2
	v_lshlrev_b32_e32 v112, 3, v109
	v_writelane_b32 v243, s12, 33
	v_lshlrev_b32_e32 v6, 2, v107
	v_add_u32_e32 v149, s8, v6
	v_writelane_b32 v243, s13, 34
	v_cmp_lt_i32_e64 s[12:13], v118, v147
	v_add_u32_e32 v151, 0, v6
	v_and_b32_e32 v159, 28, v6
	v_writelane_b32 v243, s12, 35
	v_or_b32_e32 v6, v112, v5
	s_cmpk_lt_i32 s35, 0xe00
	v_writelane_b32 v243, s13, 36
	v_cmp_gt_i32_e64 s[12:13], v7, v147
	v_or_b32_e32 v7, 3, v118
	v_or_b32_e32 v5, v118, v5
	v_writelane_b32 v243, s12, 37
	v_mad_u32_u24 v160, v5, s0, v3
	v_mul_u32_u24_e32 v5, 0x110, v6
	v_writelane_b32 v243, s13, 38
	v_cmp_gt_i32_e64 s[12:13], v7, v147
	v_or_b32_e32 v7, 16, v118
	v_mad_u32_u24 v165, v6, s0, v3
	v_writelane_b32 v243, s12, 39
	s_movk_i32 s0, 0x400
	s_cselect_b32 s3, s29, s3
	v_writelane_b32 v243, s13, 40
	v_cmp_gt_i32_e64 s[12:13], v7, v147
	v_or_b32_e32 v7, 17, v118
	v_add3_u32 v164, s2, v108, v5
	v_writelane_b32 v243, s12, 41
	s_cselect_b32 s2, s0, 0xe00
	s_cselect_b32 s0, s30, s9
	v_writelane_b32 v243, s13, 42
	v_cmp_gt_i32_e64 s[12:13], v7, v147
	v_or_b32_e32 v7, 18, v118
	s_cselect_b32 s9, s34, s28
	v_writelane_b32 v243, s12, 43
	v_mov_b32_e32 v111, 0
	v_and_b32_e32 v110, 48, v104
	v_writelane_b32 v243, s13, 44
	v_cmp_gt_i32_e64 s[12:13], v7, v147
	v_or_b32_e32 v7, 19, v118
	v_lshlrev_b32_e32 v4, 3, v1
	v_writelane_b32 v243, s12, 45
	v_or_b32_e32 v156, 8, v154
	v_lshl_add_u64 v[116:117], s[36:37], 0, v[110:111]
	v_writelane_b32 v243, s13, 46
	v_cmp_gt_i32_e64 s[12:13], v7, v147
	v_or_b32_e32 v7, 32, v118
	v_add_u32_e32 v10, 0, v110
	v_writelane_b32 v243, s12, 47
	v_lshlrev_b32_e32 v110, 4, v1
	v_or_b32_e32 v1, s9, v154
	v_writelane_b32 v243, s13, 48
	v_cmp_gt_i32_e64 s[12:13], v7, v147
	v_or_b32_e32 v7, 33, v118
	v_or_b32_e32 v157, 16, v154
	v_writelane_b32 v243, s12, 49
	v_or_b32_e32 v158, 24, v154
	v_lshlrev_b32_e32 v172, 2, v104
	v_writelane_b32 v243, s13, 50
	v_cmp_gt_i32_e64 s[12:13], v7, v147
	v_or_b32_e32 v7, 34, v118
	v_add_u32_e32 v3, 0, v172
	v_writelane_b32 v243, s12, 51
	v_add_u32_e32 v3, 0x12b00, v3
	v_and_b32_e32 v12, 0x7f, v104
	v_writelane_b32 v243, s13, 52
	v_cmp_gt_i32_e64 s[12:13], v7, v147
	v_or_b32_e32 v7, 35, v118
	v_mul_u32_u24_e32 v13, 0x110, v113
	v_writelane_b32 v243, s12, 53
	v_or_b32_e32 v128, 0xffffff00, v12
	v_mov_b32_e32 v115, v111
	v_writelane_b32 v243, s13, 54
	v_cmp_gt_i32_e64 s[12:13], v7, v147
	v_or_b32_e32 v7, 48, v118
	v_mbcnt_hi_u32_b32 v180, -1, v212
	v_writelane_b32 v243, s12, 55
	s_mov_b32 s31, 0
	v_sub_u32_e32 v129, 0xff, v119
	v_writelane_b32 v243, s13, 56
	v_cmp_gt_i32_e64 s[12:13], v7, v147
	v_or_b32_e32 v7, 49, v118
	v_sub_u32_e32 v148, 0xff, v147
	v_writelane_b32 v243, s12, 57
	s_movk_i32 s52, 0x100
	v_add_u32_e32 v150, 0x100, v149
	v_writelane_b32 v243, s13, 58
	v_cmp_gt_i32_e64 s[12:13], v7, v147
	v_or_b32_e32 v7, 50, v118
	v_cmp_lt_u32_e64 s[10:11], 15, v107
	v_writelane_b32 v243, s12, 59
	v_add_u32_e32 v153, 0xffffff00, v147
	v_add_u32_e32 v161, 0xe00, v160
	v_writelane_b32 v243, s13, 60
	v_cmp_gt_i32_e64 s[12:13], v7, v147
	v_or_b32_e32 v7, 51, v118
	v_add_u32_e32 v162, 0x1c00, v160
	v_writelane_b32 v243, s12, 61
	v_add_u32_e32 v163, 0x2a00, v160
	v_add_u32_e32 v166, 0x2200, v164
	v_writelane_b32 v243, s13, 62
	v_cmp_gt_i32_e64 s[12:13], v7, v147
	v_or_b32_e32 v7, 64, v118
	v_add_u32_e32 v167, 0xe00, v165
	v_writelane_b32 v243, s12, 63
	v_writelane_b32 v243, s36, 27
	v_add_u32_e32 v168, 0x4400, v164
	v_writelane_b32 v242, s13, 0
	v_cmp_gt_i32_e64 s[12:13], v7, v147
	v_or_b32_e32 v7, 0x41, v118
	v_writelane_b32 v243, s37, 28
	v_writelane_b32 v242, s12, 1
	v_add_u32_e32 v169, 0x1c00, v165
	v_add_u32_e32 v170, 0x6600, v164
	v_writelane_b32 v242, s13, 2
	v_cmp_gt_i32_e64 s[12:13], v7, v147
	v_or_b32_e32 v7, 0x42, v118
	v_add_u32_e32 v171, 0x2a00, v165
	v_writelane_b32 v242, s12, 3
	v_add_u32_e32 v105, 0x200, v104
	v_lshl_add_u64 v[130:131], s[36:37], 0, v[114:115]
	v_writelane_b32 v242, s13, 4
	v_cmp_gt_i32_e64 s[12:13], v7, v147
	v_or_b32_e32 v7, 0x43, v118
	v_add_u32_e32 v115, 0xfffffe00, v104
	v_writelane_b32 v242, s12, 5
	v_add_u32_e32 v176, s8, v172
	v_add_u32_e32 v177, 0x10900, v151
	v_writelane_b32 v242, s13, 6
	v_cmp_gt_i32_e64 s[12:13], v7, v147
	v_or_b32_e32 v7, 0x50, v118
	v_sub_u32_e32 v178, 0, v119
	v_writelane_b32 v242, s12, 11
	v_lshlrev_b32_e32 v132, 1, v112
	s_mov_b32 s47, 0x3f2aaaab
	v_writelane_b32 v242, s13, 12
	v_cmp_gt_i32_e64 s[12:13], v7, v147
	v_or_b32_e32 v7, 0x51, v118
	v_mov_b32_e32 v179, 0x3ecc95a3
	v_writelane_b32 v242, s12, 36
	s_mov_b32 s48, 0x3f317218
	s_mov_b32 s49, 0x7f800000
	v_writelane_b32 v242, s13, 37
	v_cmp_gt_i32_e64 s[12:13], v7, v147
	v_or_b32_e32 v7, 0x52, v118
	v_cmp_gt_i32_e64 s[60:61], v7, v147
	v_writelane_b32 v242, s12, 7
	v_or_b32_e32 v7, 0x53, v118
	v_cmp_gt_i32_e64 s[62:63], v7, v147
	v_writelane_b32 v242, s13, 8
	v_or_b32_e32 v7, 0x60, v118
	s_mov_b32 s12, 0xe00000
	v_cmp_gt_i32_e64 s[64:65], v7, v147
	v_or_b32_e32 v7, 0x61, v118
	s_cselect_b32 s12, s12, 0x700000
	s_add_u32 s3, s38, s3
	v_cmp_gt_i32_e64 s[66:67], v7, v147
	v_or_b32_e32 v7, 0x62, v118
	s_addc_u32 s13, s39, 0
	s_mul_hi_i32 s28, s12, s1
	s_mul_i32 s12, s12, s1
	v_cmp_gt_i32_e64 s[68:69], v7, v147
	v_or_b32_e32 v7, 0x63, v118
	s_add_u32 s3, s3, s12
	v_cmp_gt_i32_e64 s[70:71], v7, v147
	v_or_b32_e32 v7, 0x70, v118
	s_addc_u32 s12, s13, s28
	s_ashr_i32 s1, s0, 31
	v_cmp_gt_i32_e64 s[72:73], v7, v147
	v_or_b32_e32 v7, 0x71, v118
	s_lshl_b64 s[0:1], s[0:1], 1
	v_cmp_gt_i32_e64 s[74:75], v7, v147
	v_or_b32_e32 v7, 0x72, v118
	s_add_u32 s0, s3, s0
	v_cmp_gt_i32_e64 s[76:77], v7, v147
	v_or_b32_e32 v7, 0x73, v118
	s_addc_u32 s1, s12, s1
	v_cmp_gt_i32_e64 s[78:79], v7, v147
	v_lshl_add_u64 v[6:7], s[0:1], 0, v[110:111]
	v_mad_i64_i32 v[8:9], s[0:1], s2, v1, 0
	v_or_b32_e32 v1, s9, v156
	v_lshl_add_u64 v[120:121], v[8:9], 1, v[6:7]
	v_mad_i64_i32 v[8:9], s[0:1], s2, v1, 0
	v_or_b32_e32 v1, s9, v157
	v_lshl_add_u64 v[122:123], v[8:9], 1, v[6:7]
	v_mad_i64_i32 v[8:9], s[0:1], s2, v1, 0
	v_or_b32_e32 v1, s9, v158
	v_lshl_add_u64 v[124:125], v[8:9], 1, v[6:7]
	v_mad_i64_i32 v[8:9], s[0:1], s2, v1, 0
	v_max_i32_e32 v1, 0x700, v104
	v_sub_u32_e32 v1, v1, v104
	v_add_u32_e32 v1, 0x1ff, v1
	v_lshl_add_u64 v[126:127], v[8:9], 1, v[6:7]
	v_lshlrev_b32_e32 v8, 2, v1
	s_movk_i32 s0, 0xdff
	v_and_b32_e32 v8, 0xfffff800, v8
	v_lshrrev_b32_e32 v5, 9, v1
	v_cmp_lt_u32_e32 vcc, s0, v1
	v_cmp_gt_u32_e64 s[0:1], 2.0, v1
	v_add_u32_e32 v1, v3, v8
	v_writelane_b32 v242, s38, 29
	v_add_u32_e32 v6, 1, v5
	v_add_u32_e32 v5, -1, v5
	v_cmp_ge_u32_e64 s[2:3], v1, v3
	v_writelane_b32 v242, s39, 39
	s_and_b64 s[0:1], s[2:3], s[0:1]
	v_cmp_lt_u32_e64 s[2:3], 1, v5
	v_lshrrev_b32_e32 v7, 1, v5
	v_and_b32_e32 v5, 2, v5
	v_writelane_b32 v242, s2, 45
	v_and_b32_e32 v3, 0xfffffe, v6
	s_and_b64 s[0:1], vcc, s[0:1]
	v_writelane_b32 v242, s3, 46
	v_cmp_eq_u32_e64 s[2:3], 0, v5
	v_lshl_add_u32 v173, v3, 9, v104
	v_add_u32_e32 v7, 1, v7
	v_writelane_b32 v242, s2, 47
	v_mov_b32_e32 v1, v128
	v_and_b32_e32 v174, -2, v7
	v_writelane_b32 v242, s3, 48
	v_cmp_ne_u32_e64 s[2:3], v6, v3
	v_lshl_add_u32 v3, v104, 4, 0
	v_add_u32_e32 v175, 0xc000, v3
	v_writelane_b32 v242, s2, 49
	v_bfrev_b32_e32 v6, 0.5
	s_sub_i32 s46, 0, s44
	v_writelane_b32 v242, s3, 50
	v_writelane_b32 v242, s0, 51
	s_mov_b32 s50, 0x33800000
	v_lshlrev_b32_e32 v134, 2, v118
	v_writelane_b32 v242, s1, 52
	s_add_i32 s0, 0, 0x25de0
	v_writelane_b32 v243, s0, 14
	s_add_i32 s0, 0, 0x25db8
	v_writelane_b32 v242, s0, 23
	s_add_i32 s0, 0, 0x25dd0
	v_writelane_b32 v242, s0, 21
	s_add_i32 s0, 0, 0x25da8
	v_writelane_b32 v243, s0, 19
	s_add_i32 s0, 0, 0x25dd8
	v_writelane_b32 v243, s0, 20
	s_add_i32 s0, 0, 0x25db0
	v_writelane_b32 v242, s0, 10
	s_add_i32 s0, s43, 0x820
	v_writelane_b32 v242, s0, 31
	s_add_i32 s0, s43, 0xc30
	v_writelane_b32 v242, s0, 33
	s_add_i32 s0, s43, 0x1040
	v_writelane_b32 v242, s0, 34
	s_add_i32 s0, s43, 0x1450
	v_writelane_b32 v242, s0, 35
	s_add_i32 s0, s43, 0x1860
	v_add_u32_e32 v181, v2, v114
	s_xor_b64 s[28:29], s[84:85], -1
	v_lshlrev_b32_e32 v110, 1, v4
	v_writelane_b32 v242, s0, 38
	s_add_i32 s0, s43, 0x1c70
	v_add_u32_e32 v182, v11, v13
	v_mov_b32_e32 v2, v111
	v_mov_b32_e32 v3, v111
	v_mov_b32_e32 v4, v111
	v_mov_b32_e32 v5, v111
	v_mov_b32_e32 v136, 0x3f317218
	v_mov_b32_e32 v183, 0x7f800000
	v_mov_b32_e32 v184, 0x7fc00000
	v_mov_b32_e32 v185, 0xff800000
	v_lshl_or_b32 v186, v180, 2, v6
	v_add_u32_e32 v187, v10, v13
	v_mov_b32_e32 v188, 0x7c
	v_writelane_b32 v242, s0, 24
	s_branch .LBB0_2012

.LBB0_3626:
	s_or_b64 exec, exec, s[0:1]
	s_load_dwordx2 s[0:1], s[80:81], 0xf0
	v_mov_b32_e32 v104, v0
	s_waitcnt lgkmcnt(0)
	s_barrier
	v_mov_b32_e32 v1, s0
	v_mov_b32_e32 v2, s1
	s_add_i32 s0, 0, 0x25d38
	v_readfirstlane_b32 s2, v2
	v_mov_b32_e32 v2, s79
	v_mov_b32_e32 v4, s77
	v_mov_b32_e32 v5, s78
	v_mov_b32_e32 v2, s0
	ds_read_b64 v[2:3], v2
	v_readfirstlane_b32 s52, v4
	v_readfirstlane_b32 s3, v1
	v_readfirstlane_b32 s53, v5
	s_mov_b32 s35, 0
	s_waitcnt lgkmcnt(0)
	v_readfirstlane_b32 s0, v2
	v_readfirstlane_b32 s1, v3
	s_cmpk_gt_i32 s52, 0xff
	v_writelane_b32 v243, s0, 27
	v_readfirstlane_b32 s10, v104
	s_nop 0
	v_writelane_b32 v243, s1, 28
	s_cbranch_scc1 .LBB0_3854
	v_readfirstlane_b32 s98, v0
	s_nop 3
	s_cmp_gt_u32 s98, 255
	s_cbranch_scc1 .Lp4oldprio2
	s_setprio 1
.Lp4oldprio2:
	s_add_u32 s4, s3, 0x7400000
	s_addc_u32 s5, s2, 0
	s_add_u32 s44, s3, 0x17e00000
	s_addc_u32 s45, s2, 0
	s_add_u32 s0, s3, 0x300000
	v_writelane_b32 v242, s0, 45
	s_addc_u32 s0, s2, 0
	v_writelane_b32 v242, s0, 47
	s_add_u32 s0, s3, 0x1a200000
	v_writelane_b32 v243, s0, 16
	s_addc_u32 s0, s2, 0
	s_ashr_i32 s28, s10, 6
	v_writelane_b32 v243, s0, 17
	s_mul_i32 s0, s28, 0x2080
	s_add_i32 s0, s0, 0
	s_add_i32 s48, s0, 0x14f00
	s_lshl_b32 s0, s52, 3
	s_add_i32 s46, s28, s0
	s_lshl_b32 s33, s53, 3
	s_cmpk_eq_i32 s53, 0x100
	s_cselect_b64 s[8:9], -1, 0
	s_and_b64 s[0:1], s[8:9], exec
	s_movk_i32 s1, 0x330
	v_cmp_gt_i32_e64 s[6:7], s1, v104
	v_and_b32_e32 v1, 3, v104
	s_cselect_b32 s16, 0x4800, 0
	v_writelane_b32 v242, s6, 13
	s_cselect_b32 s0, 3, 0
	s_lshl_b32 s17, s28, 4
	v_writelane_b32 v242, s7, 14
	v_cmp_eq_u32_e64 s[6:7], 0, v1
	v_ashrrev_i32_e32 v119, 2, v104
	s_movk_i32 s1, 0x70
	v_writelane_b32 v242, s6, 15
	s_cmp_gt_u32 s10, 63
	v_and_b32_e32 v107, 63, v104
	v_writelane_b32 v242, s7, 16
	s_movk_i32 s6, 0x8ff
	v_cmp_lt_i32_e64 s[6:7], s6, v104
	v_mul_lo_u32 v2, v119, s1
	v_add_u32_e32 v106, 0, v2
	v_writelane_b32 v242, s6, 17
	v_lshlrev_b32_e32 v2, 1, v107
	s_movk_i32 s14, 0xa0
	v_writelane_b32 v242, s7, 18
	s_cselect_b64 s[6:7], -1, 0
	s_cmp_lt_u32 s10, 64
	s_cselect_b64 s[10:11], -1, 0
	s_add_i32 s29, 0, 0x10700
	v_lshlrev_b32_e32 v108, 3, v1
	v_sub_u32_e32 v152, 0, v2
	v_mad_u64_u32 v[2:3], s[14:15], v119, s14, v[106:107]
	v_lshlrev_b32_e32 v114, 4, v1
	s_add_u32 s47, s3, 0x2ce00000
	v_and_b32_e32 v1, 7, v104
	v_bfe_u32 v154, v104, 3, 3
	s_addc_u32 s50, s2, 0
	v_mul_u32_u24_e32 v3, 0x410, v1
	v_lshlrev_b32_e32 v6, 2, v154
	s_add_i32 s2, 0, 0x8800
	v_add3_u32 v155, s48, v3, v6
	v_add_u32_e32 v3, s2, v108
	s_lshl_b32 s3, s28, 5
	s_mul_i32 s2, s53, 0x88
	s_add_i32 s3, s3, 0
	s_add_i32 s20, s46, s2
	s_cmp_lt_i32 s20, s16
	v_bfe_u32 v109, v104, 4, 2
	s_cselect_b64 s[42:43], -1, 0
	s_cmp_ge_i32 s20, s16
	v_and_b32_e32 v113, 15, v104
	v_lshlrev_b32_e32 v118, 2, v109
	s_cselect_b64 s[14:15], -1, 0
	v_or_b32_e32 v147, s17, v113
	v_sub_u32_e32 v244, v147, v118
	v_subrev_u32_e32 v245, 64, v244
	v_or_b32_e32 v8, s17, v118
	s_and_b64 s[16:17], s[8:9], s[14:15]
	s_and_b64 s[16:17], s[16:17], exec
	s_cselect_b32 s2, 0xffffb800, 0
	s_add_i32 s21, s2, s20
	s_bfe_i32 s2, s0, 0x10000
	s_and_b32 s16, s0, 1
	v_writelane_b32 v242, s10, 41
	s_bitcmp1_b32 s0, 0
	s_cselect_b64 s[18:19], -1, 0
	v_writelane_b32 v242, s11, 42
	s_cmp_eq_u32 s16, 0
	v_writelane_b32 v242, s18, 31
	s_cselect_b64 s[16:17], -1, 0
	s_mul_hi_i32 s22, s21, 0x30c30c31
	v_writelane_b32 v242, s19, 32
	s_and_b64 s[18:19], s[16:17], exec
	s_mov_b32 s23, 0xc600000
	s_mov_b32 s18, 0xb800000
	s_cselect_b32 s34, s23, 0x8000000
	s_cselect_b32 s54, s18, 0x1000000
	s_or_b64 s[14:15], s[16:17], s[14:15]
	s_lshr_b32 s16, s22, 31
	s_ashr_i32 s30, s22, 10
	s_add_i32 s30, s30, s16
	s_mul_i32 s16, s30, 0xffffeb00
	s_add_i32 s41, s16, s21
	s_and_b64 s[16:17], s[14:15], exec
	s_cselect_b32 s31, s23, 0x8000000
	s_lshl_b32 s16, s41, 1
	s_add_i32 s16, s16, 0x7fffe400
	s_and_b32 s36, s16, 0x7fffffc0
	s_lshl_b32 s16, s20, 5
	s_and_b32 s37, s16, 0x3e0
	s_mul_hi_i32 s19, s41, 0x92492493
	s_and_b64 s[14:15], s[14:15], exec
	s_cselect_b32 s38, s18, 0x1000000
	s_add_i32 s19, s19, s41
	s_lshr_b32 s14, s19, 31
	s_ashr_i32 s15, s19, 7
	s_add_i32 s14, s15, s14
	s_mul_i32 s15, s14, 0xe0
	s_lshl_b32 s39, s14, 6
	s_sub_i32 s14, s41, s15
	s_lshl_b32 s40, s14, 5
	s_cmp_gt_i32 s28, -1
	s_cselect_b64 s[84:85], -1, 0
	s_cmp_gt_i32 s28, 0
	s_cselect_b64 s[14:15], -1, 0
	s_cmp_gt_i32 s28, 1
	s_cselect_b64 s[16:17], -1, 0
	s_cmp_gt_i32 s28, 2
	s_cselect_b64 s[18:19], -1, 0
	s_cmp_gt_i32 s28, 3
	s_cselect_b64 s[20:21], -1, 0
	s_cmp_gt_i32 s28, 4
	s_cselect_b64 s[22:23], -1, 0
	s_cmp_gt_i32 s28, 5
	s_cselect_b64 s[24:25], -1, 0
	s_cmp_gt_i32 s28, 6
	s_cselect_b64 s[26:27], -1, 0
	s_and_b64 s[42:43], s[8:9], s[42:43]
	v_writelane_b32 v242, s42, 43
	v_lshl_add_u32 v12, v8, 1, 0
	v_or_b32_e32 v8, 2, v118
	v_writelane_b32 v242, s43, 44
	v_cmp_gt_i32_e64 s[42:43], v118, v147
	v_bfe_u32 v5, v104, 2, 2
	v_lshlrev_b32_e32 v112, 3, v109
	v_writelane_b32 v243, s42, 31
	v_lshlrev_b32_e32 v7, 2, v107
	v_add_u32_e32 v149, s29, v7
	v_writelane_b32 v243, s43, 32
	v_cmp_lt_i32_e64 s[42:43], v118, v147
	v_add_u32_e32 v151, 0, v7
	v_and_b32_e32 v159, 28, v7
	v_writelane_b32 v243, s42, 33
	v_or_b32_e32 v7, v112, v5
	v_or_b32_e32 v5, v118, v5
	v_writelane_b32 v243, s43, 34
	v_cmp_gt_i32_e64 s[42:43], v8, v147
	v_or_b32_e32 v8, 3, v118
	s_cmpk_lt_i32 s41, 0xe00
	v_writelane_b32 v243, s42, 35
	v_mad_u32_u24 v160, v5, s1, v3
	v_mul_u32_u24_e32 v5, 0x110, v7
	v_writelane_b32 v243, s43, 36
	v_cmp_gt_i32_e64 s[42:43], v8, v147
	v_or_b32_e32 v8, 16, v118
	v_add3_u32 v164, s3, v108, v5
	v_writelane_b32 v243, s42, 37
	s_cselect_b32 s3, s40, s37
	s_mov_b32 s37, 0xe00000
	v_writelane_b32 v243, s43, 38
	v_cmp_gt_i32_e64 s[42:43], v8, v147
	v_or_b32_e32 v8, 17, v118
	v_mad_u32_u24 v165, v7, s1, v3
	v_writelane_b32 v243, s42, 39
	s_movk_i32 s1, 0x400
	s_cselect_b32 s31, s38, s31
	v_writelane_b32 v243, s43, 40
	v_cmp_gt_i32_e64 s[42:43], v8, v147
	v_or_b32_e32 v8, 18, v118
	s_cselect_b32 s37, s37, 0x700000
	v_writelane_b32 v243, s42, 41
	s_cselect_b32 s1, s1, 0xe00
	s_cselect_b32 s36, s39, s36
	v_writelane_b32 v243, s43, 42
	v_cmp_gt_i32_e64 s[42:43], v8, v147
	v_or_b32_e32 v8, 19, v118
	s_mul_hi_i32 s38, s37, s30
	v_writelane_b32 v243, s42, 43
	s_mul_i32 s37, s37, s30
	s_add_u32 s30, s47, s31
	v_writelane_b32 v243, s43, 44
	v_cmp_gt_i32_e64 s[42:43], v8, v147
	v_or_b32_e32 v8, 32, v118
	s_addc_u32 s31, s50, 0
	v_writelane_b32 v243, s42, 45
	s_add_u32 s39, s30, s37
	s_addc_u32 s38, s31, s38
	v_writelane_b32 v243, s43, 46
	v_cmp_gt_i32_e64 s[42:43], v8, v147
	v_or_b32_e32 v8, 33, v118
	s_ashr_i32 s37, s36, 31
	v_writelane_b32 v243, s42, 47
	s_lshl_b64 s[30:31], s[36:37], 1
	v_mov_b32_e32 v111, 0
	v_writelane_b32 v243, s43, 48
	v_cmp_gt_i32_e64 s[42:43], v8, v147
	v_or_b32_e32 v8, 34, v118
	v_and_b32_e32 v110, 48, v104
	v_writelane_b32 v243, s42, 49
	s_add_u32 s30, s39, s30
	v_lshlrev_b32_e32 v4, 3, v1
	v_writelane_b32 v243, s43, 50
	v_cmp_gt_i32_e64 s[42:43], v8, v147
	v_or_b32_e32 v8, 35, v118
	v_or_b32_e32 v156, 8, v154
	v_writelane_b32 v243, s42, 51
	v_lshl_add_u64 v[116:117], s[44:45], 0, v[110:111]
	v_add_u32_e32 v6, 0, v110
	v_writelane_b32 v243, s43, 52
	v_cmp_gt_i32_e64 s[42:43], v8, v147
	v_or_b32_e32 v8, 48, v118
	s_addc_u32 s31, s38, s31
	v_writelane_b32 v243, s42, 53
	v_lshlrev_b32_e32 v110, 4, v1
	v_or_b32_e32 v1, s3, v154
	v_writelane_b32 v243, s43, 54
	v_cmp_gt_i32_e64 s[42:43], v8, v147
	v_or_b32_e32 v8, 49, v118
	v_or_b32_e32 v157, 16, v154
	v_writelane_b32 v243, s42, 55
	v_or_b32_e32 v158, 24, v154
	s_lshr_b32 s0, s0, 1
	v_writelane_b32 v243, s43, 56
	v_cmp_gt_i32_e64 s[42:43], v8, v147
	v_or_b32_e32 v8, 50, v118
	v_lshlrev_b32_e32 v172, 2, v104
	v_writelane_b32 v243, s42, 57
	v_add_u32_e32 v3, 0, v172
	v_add_u32_e32 v3, 0x12b00, v3
	v_writelane_b32 v243, s43, 58
	v_cmp_gt_i32_e64 s[42:43], v8, v147
	v_or_b32_e32 v8, 51, v118
	v_and_b32_e32 v13, 0x7f, v104
	v_writelane_b32 v243, s42, 59
	v_mul_u32_u24_e32 v14, 0x110, v113
	v_or_b32_e32 v128, 0xffffff00, v13
	v_writelane_b32 v243, s43, 60
	v_cmp_gt_i32_e64 s[42:43], v8, v147
	v_or_b32_e32 v8, 64, v118
	v_mov_b32_e32 v115, v111
	v_writelane_b32 v243, s42, 61
	v_mbcnt_hi_u32_b32 v180, -1, v212
	s_movk_i32 s49, 0x100
	v_writelane_b32 v243, s43, 62
	v_cmp_gt_i32_e64 s[42:43], v8, v147
	v_or_b32_e32 v8, 0x41, v118
	v_sub_u32_e32 v129, 0xff, v119
	v_writelane_b32 v243, s42, 63
	v_writelane_b32 v243, s34, 14
	s_mov_b32 s55, s35
	v_writelane_b32 v242, s43, 0
	v_cmp_gt_i32_e64 s[42:43], v8, v147
	v_or_b32_e32 v8, 0x42, v118
	v_writelane_b32 v243, s35, 15
	v_writelane_b32 v242, s42, 1
	v_sub_u32_e32 v148, 0xff, v147
	v_add_u32_e32 v150, 0x100, v149
	v_writelane_b32 v242, s43, 2
	v_cmp_gt_i32_e64 s[42:43], v8, v147
	v_or_b32_e32 v8, 0x43, v118
	v_cmp_lt_u32_e64 s[10:11], 15, v107
	v_writelane_b32 v242, s42, 3
	v_cmp_eq_u32_e64 s[12:13], 0, v107
	v_add_u32_e32 v153, 0xffffff00, v147
	v_writelane_b32 v242, s43, 4
	v_cmp_gt_i32_e64 s[42:43], v8, v147
	v_or_b32_e32 v8, 0x50, v118
	v_add_u32_e32 v161, 0xe00, v160
	v_writelane_b32 v242, s42, 5
	v_add_u32_e32 v162, 0x1c00, v160
	v_add_u32_e32 v163, 0x2a00, v160
	v_writelane_b32 v242, s43, 6
	v_cmp_gt_i32_e64 s[42:43], v8, v147
	v_or_b32_e32 v8, 0x51, v118
	v_cmp_gt_i32_e64 s[58:59], v8, v147
	v_or_b32_e32 v8, 0x52, v118
	v_cmp_gt_i32_e64 s[60:61], v8, v147
	v_or_b32_e32 v8, 0x53, v118
	v_cmp_gt_i32_e64 s[62:63], v8, v147
	v_or_b32_e32 v8, 0x60, v118
	v_cmp_gt_i32_e64 s[64:65], v8, v147
	v_or_b32_e32 v8, 0x61, v118
	v_cmp_gt_i32_e64 s[66:67], v8, v147
	v_or_b32_e32 v8, 0x62, v118
	v_cmp_gt_i32_e64 s[68:69], v8, v147
	v_or_b32_e32 v8, 0x63, v118
	v_cmp_gt_i32_e64 s[70:71], v8, v147
	v_or_b32_e32 v8, 0x70, v118
	v_cmp_gt_i32_e64 s[72:73], v8, v147
	v_or_b32_e32 v8, 0x71, v118
	v_cmp_gt_i32_e64 s[74:75], v8, v147
	v_or_b32_e32 v8, 0x72, v118
	v_cmp_gt_i32_e64 s[76:77], v8, v147
	v_or_b32_e32 v8, 0x73, v118
	v_writelane_b32 v242, s42, 11
	v_cmp_gt_i32_e64 s[78:79], v8, v147
	v_lshl_add_u64 v[8:9], s[30:31], 0, v[110:111]
	v_mad_i64_i32 v[10:11], s[30:31], s1, v1, 0
	v_or_b32_e32 v1, s3, v156
	v_writelane_b32 v242, s43, 12
	v_lshl_add_u64 v[120:121], v[10:11], 1, v[8:9]
	v_mad_i64_i32 v[10:11], s[30:31], s1, v1, 0
	v_or_b32_e32 v1, s3, v157
	v_writelane_b32 v242, s47, 9
	v_lshl_add_u64 v[122:123], v[10:11], 1, v[8:9]
	v_mad_i64_i32 v[10:11], s[30:31], s1, v1, 0
	v_or_b32_e32 v1, s3, v158
	v_writelane_b32 v242, s50, 30
	v_lshl_add_u64 v[124:125], v[10:11], 1, v[8:9]
	v_mad_i64_i32 v[10:11], s[30:31], s1, v1, 0
	s_lshl_b32 s1, s46, 5
	v_writelane_b32 v242, s46, 19
	s_and_b32 s1, s1, 0x3e0
	v_max_i32_e32 v1, 0x700, v104
	v_writelane_b32 v242, s1, 36
	v_sub_u32_e32 v1, v1, v104
	v_writelane_b32 v242, s54, 39
	s_and_b32 s1, s2, 3
	v_add_u32_e32 v1, 0x1ff, v1
	v_lshl_add_u64 v[126:127], v[10:11], 1, v[8:9]
	v_writelane_b32 v242, s55, 40
	s_lshl_b32 s0, s0, s1
	v_lshlrev_b32_e32 v9, 2, v1
	v_writelane_b32 v242, s0, 33
	s_movk_i32 s0, 0xdff
	v_and_b32_e32 v9, 0xfffff800, v9
	v_lshrrev_b32_e32 v5, 9, v1
	v_cmp_lt_u32_e32 vcc, s0, v1
	v_cmp_gt_u32_e64 s[0:1], 2.0, v1
	v_add_u32_e32 v1, v3, v9
	v_add_u32_e32 v7, 1, v5
	v_add_u32_e32 v5, -1, v5
	v_cmp_ge_u32_e64 s[2:3], v1, v3
	s_and_b64 s[0:1], s[2:3], s[0:1]
	v_cmp_lt_u32_e64 s[2:3], 1, v5
	v_lshrrev_b32_e32 v8, 1, v5
	v_and_b32_e32 v5, 2, v5
	v_writelane_b32 v242, s2, 53
	v_and_b32_e32 v3, 0xfffffe, v7
	s_and_b64 s[0:1], vcc, s[0:1]
	v_writelane_b32 v242, s3, 54
	v_cmp_eq_u32_e64 s[2:3], 0, v5
	s_lshl_b32 s43, s53, 4
	v_lshl_add_u32 v173, v3, 9, v104
	v_writelane_b32 v242, s2, 55
	v_add_u32_e32 v8, 1, v8
	v_add_u32_e32 v166, 0x2200, v164
	v_writelane_b32 v242, s3, 56
	v_cmp_ne_u32_e64 s[2:3], v7, v3
	v_lshl_add_u32 v3, v104, 4, 0
	v_add_u32_e32 v175, 0xc000, v3
	v_writelane_b32 v242, s2, 57
	v_bfrev_b32_e32 v7, 0.5
	v_add_u32_e32 v167, 0xe00, v165
	v_writelane_b32 v242, s3, 58
	v_writelane_b32 v242, s0, 49
	v_add_u32_e32 v168, 0x4400, v164
	v_add_u32_e32 v169, 0x1c00, v165
	v_writelane_b32 v242, s1, 50
	v_writelane_b32 v242, s44, 25
	s_sub_i32 s0, 0, s43
	s_lshl_b32 s1, s28, 1
	v_writelane_b32 v242, s45, 26
	v_writelane_b32 v242, s0, 23
	s_lshl_b32 s0, s52, 4
	s_add_i32 s0, s0, s1
	s_add_i32 s0, s0, 0x7fffe400
	v_writelane_b32 v242, s0, 51
	s_add_i32 s0, 0, 0x25de0
	v_writelane_b32 v242, s0, 21
	s_add_i32 s0, 0, 0x25db8
	v_writelane_b32 v243, s0, 19
	s_add_i32 s0, 0, 0x25dd0
	v_writelane_b32 v243, s0, 20
	s_add_i32 s0, 0, 0x25da8
	v_writelane_b32 v242, s0, 10
	s_add_i32 s0, 0, 0x25dd8
	v_writelane_b32 v243, s0, 21
	s_add_i32 s0, 0, 0x25db0
	v_writelane_b32 v243, s0, 23
	s_add_i32 s0, s48, 0x820
	v_writelane_b32 v242, s0, 34
	s_add_i32 s0, s48, 0xc30
	v_writelane_b32 v242, s0, 35
	s_add_i32 s0, s48, 0x1040
	v_writelane_b32 v242, s0, 38
	s_add_i32 s0, s48, 0x1450
	v_writelane_b32 v242, s0, 24
	s_add_i32 s0, s48, 0x1860
	v_writelane_b32 v242, s0, 27
	v_add_u32_e32 v170, 0x6600, v164
	v_add_u32_e32 v171, 0x2a00, v165
	v_mov_b32_e32 v1, v128
	v_add_u32_e32 v105, 0x200, v104
	v_and_b32_e32 v174, -2, v8
	v_lshl_add_u64 v[130:131], s[44:45], 0, v[114:115]
	v_add_u32_e32 v115, 0xfffffe00, v104
	v_add_u32_e32 v176, s29, v172
	s_sub_i32 s42, 0, s33
	v_add_u32_e32 v177, 0x10900, v151
	v_sub_u32_e32 v178, 0, v119
	s_movk_i32 s55, 0x3000
	v_lshlrev_b32_e32 v132, 1, v112
	s_mov_b32 s44, 0x3f2aaaab
	v_mov_b32_e32 v179, 0x3ecc95a3
	s_mov_b32 s45, 0x3f317218
	s_mov_b32 s46, 0x7f800000
	s_mov_b32 s47, 0x33800000
	v_lshlrev_b32_e32 v134, 2, v118
	v_add_u32_e32 v181, v2, v114
	s_xor_b64 s[28:29], s[8:9], -1
	v_lshlrev_b32_e32 v110, 1, v4
	v_writelane_b32 v242, s48, 7
	s_add_i32 s0, s48, 0x1c70
	v_add_u32_e32 v182, v12, v14
	v_mov_b32_e32 v2, v111
	v_mov_b32_e32 v3, v111
	v_mov_b32_e32 v4, v111
	v_mov_b32_e32 v5, v111
	v_mov_b32_e32 v136, 0x3f317218
	v_mov_b32_e32 v183, 0x7f800000
	v_mov_b32_e32 v184, 0x7fc00000
	v_mov_b32_e32 v185, 0xff800000
	v_lshl_or_b32 v186, v180, 2, v7
	v_add_u32_e32 v187, v6, v14
	v_mov_b32_e32 v188, 0x7c
	v_writelane_b32 v242, s0, 29
	v_writelane_b32 v243, s53, 29
	s_branch .LBB0_3629

.LBB0_4989:
	s_or_b64 exec, exec, s[0:1]
	v_readlane_b32 s0, v243, 8
	v_readlane_b32 s1, v243, 9
	v_mov_b32_e32 v104, v0
	s_waitcnt lgkmcnt(0)
	v_mov_b32_e32 v1, s0
	v_mov_b32_e32 v2, s1
	s_barrier
	s_add_i32 s0, 0, 0x25d38
	v_readfirstlane_b32 s12, v2
	v_mov_b32_e32 v2, s79
	v_mov_b32_e32 v4, s77
	v_mov_b32_e32 v5, s78
	v_mov_b32_e32 v2, s0
	ds_read_b64 v[2:3], v2
	v_readfirstlane_b32 s50, v4
	v_readfirstlane_b32 s13, v1
	v_readfirstlane_b32 s44, v5
	s_mov_b32 s31, 0
	s_waitcnt lgkmcnt(0)
	v_readfirstlane_b32 s0, v2
	v_readfirstlane_b32 s1, v3
	s_cmpk_gt_i32 s50, 0xff
	v_writelane_b32 v243, s0, 27
	v_readfirstlane_b32 s8, v104
	s_nop 0
	v_writelane_b32 v243, s1, 28
	s_cbranch_scc1 .LBB0_5217
	v_readfirstlane_b32 s98, v0
	s_nop 3
	s_cmp_gt_u32 s98, 255
	s_cbranch_scc1 .Lp4oldprio3
	s_setprio 1
.Lp4oldprio3:
	s_add_u32 s0, s13, 0x7400000
	s_addc_u32 s1, s12, 0
	s_add_u32 s46, s13, 0x17e00000
	s_addc_u32 s47, s12, 0
	s_add_u32 s2, s13, 0x300000
	v_writelane_b32 v243, s80, 12
	v_writelane_b32 v242, s2, 45
	s_addc_u32 s2, s12, 0
	v_writelane_b32 v243, s81, 13
	v_writelane_b32 v242, s2, 47
	s_add_u32 s2, s13, 0x1a200000
	v_writelane_b32 v243, s2, 16
	s_addc_u32 s2, s12, 0
	s_ashr_i32 s26, s8, 6
	v_writelane_b32 v243, s2, 17
	s_mul_i32 s2, s26, 0x2080
	s_add_i32 s2, s2, 0
	s_add_i32 s48, s2, 0x14f00
	s_lshl_b32 s2, s50, 3
	s_add_i32 s45, s26, s2
	s_lshl_b32 s33, s44, 3
	s_cmpk_eq_i32 s44, 0x100
	s_cselect_b64 s[6:7], -1, 0
	s_and_b64 s[2:3], s[6:7], exec
	s_movk_i32 s3, 0x330
	v_cmp_gt_i32_e64 s[4:5], s3, v104
	v_and_b32_e32 v1, 3, v104
	s_cselect_b32 s16, 0x4800, 0
	v_writelane_b32 v242, s4, 13
	s_cselect_b32 s2, 3, 0
	s_lshl_b32 s17, s26, 4
	v_writelane_b32 v242, s5, 14
	v_cmp_eq_u32_e64 s[4:5], 0, v1
	v_ashrrev_i32_e32 v119, 2, v104
	s_movk_i32 s3, 0x70
	v_writelane_b32 v242, s4, 15
	s_cmp_gt_u32 s8, 63
	v_and_b32_e32 v107, 63, v104
	v_writelane_b32 v242, s5, 16
	s_movk_i32 s4, 0x8ff
	v_cmp_lt_i32_e64 s[4:5], s4, v104
	v_mul_lo_u32 v2, v119, s3
	v_add_u32_e32 v106, 0, v2
	v_writelane_b32 v242, s4, 17
	v_lshlrev_b32_e32 v2, 1, v107
	s_movk_i32 s14, 0xa0
	v_writelane_b32 v242, s5, 18
	s_cselect_b64 s[4:5], -1, 0
	s_cmp_lt_u32 s8, 64
	s_cselect_b64 s[8:9], -1, 0
	s_add_i32 s27, 0, 0x10700
	s_sub_i32 s18, 0, s16
	v_lshlrev_b32_e32 v108, 3, v1
	v_sub_u32_e32 v152, 0, v2
	v_mad_u64_u32 v[2:3], s[14:15], v119, s14, v[106:107]
	v_lshlrev_b32_e32 v114, 4, v1
	s_add_u32 s51, s13, 0x2ce00000
	v_and_b32_e32 v1, 7, v104
	v_bfe_u32 v154, v104, 3, 3
	s_addc_u32 s52, s12, 0
	v_mul_u32_u24_e32 v3, 0x410, v1
	v_lshlrev_b32_e32 v6, 2, v154
	s_add_i32 s12, 0, 0x8800
	v_add3_u32 v155, s48, v3, v6
	v_add_u32_e32 v3, s12, v108
	s_lshl_b32 s29, s26, 5
	s_mul_i32 s12, s44, 0x88
	s_add_i32 s29, s29, 0
	s_add_i32 s19, s45, s12
	s_cmp_lt_i32 s19, s16
	s_cselect_b64 s[42:43], -1, 0
	s_cmp_ge_i32 s19, s16
	s_cselect_b64 s[12:13], -1, 0
	s_and_b64 s[14:15], s[12:13], exec
	s_cselect_b32 s14, s18, s16
	v_bfe_u32 v109, v104, 4, 2
	s_add_i32 s18, s14, s19
	s_bfe_i32 s28, s2, 0x10000
	s_and_b32 s14, s2, 1
	v_and_b32_e32 v113, 15, v104
	v_writelane_b32 v242, s8, 41
	v_lshlrev_b32_e32 v118, 2, v109
	s_bitcmp1_b32 s2, 0
	v_or_b32_e32 v147, s17, v113
	v_sub_u32_e32 v244, v147, v118
	v_subrev_u32_e32 v245, 64, v244
	v_writelane_b32 v242, s9, 42
	v_or_b32_e32 v8, s17, v118
	s_cselect_b64 s[16:17], -1, 0
	s_cmp_eq_u32 s14, 0
	v_writelane_b32 v242, s16, 31
	s_cselect_b64 s[14:15], -1, 0
	s_mul_hi_i32 s20, s18, 0x30c30c31
	v_writelane_b32 v242, s17, 32
	s_and_b64 s[16:17], s[14:15], exec
	s_mov_b32 s21, 0xc600000
	s_mov_b32 s16, 0xb800000
	s_cselect_b32 s30, s21, 0x8000000
	s_cselect_b32 s54, s16, 0x1000000
	s_or_b64 s[12:13], s[14:15], s[12:13]
	s_lshr_b32 s14, s20, 31
	s_ashr_i32 s34, s20, 10
	s_add_i32 s34, s34, s14
	s_mul_i32 s14, s34, 0xffffeb00
	s_add_i32 s41, s14, s18
	s_and_b64 s[14:15], s[12:13], exec
	s_cselect_b32 s35, s21, 0x8000000
	s_lshl_b32 s14, s41, 1
	s_add_i32 s14, s14, 0x7fffe400
	s_and_b32 s36, s14, 0x7fffffc0
	s_lshl_b32 s14, s19, 5
	s_and_b32 s37, s14, 0x3e0
	s_mul_hi_i32 s17, s41, 0x92492493
	s_and_b64 s[12:13], s[12:13], exec
	s_cselect_b32 s38, s16, 0x1000000
	s_add_i32 s17, s17, s41
	s_lshr_b32 s12, s17, 31
	s_ashr_i32 s13, s17, 7
	s_add_i32 s12, s13, s12
	s_mul_i32 s13, s12, 0xe0
	s_lshl_b32 s39, s12, 6
	s_sub_i32 s12, s41, s13
	s_lshl_b32 s40, s12, 5
	s_cmp_gt_i32 s26, -1
	s_cselect_b64 s[82:83], -1, 0
	s_cmp_gt_i32 s26, 0
	s_cselect_b64 s[12:13], -1, 0
	s_cmp_gt_i32 s26, 1
	s_cselect_b64 s[14:15], -1, 0
	s_cmp_gt_i32 s26, 2
	s_cselect_b64 s[16:17], -1, 0
	s_cmp_gt_i32 s26, 3
	s_cselect_b64 s[18:19], -1, 0
	s_cmp_gt_i32 s26, 4
	s_cselect_b64 s[20:21], -1, 0
	s_cmp_gt_i32 s26, 5
	s_cselect_b64 s[22:23], -1, 0
	s_cmp_gt_i32 s26, 6
	s_cselect_b64 s[24:25], -1, 0
	s_and_b64 s[42:43], s[6:7], s[42:43]
	v_writelane_b32 v242, s42, 43
	v_lshl_add_u32 v12, v8, 1, 0
	v_or_b32_e32 v8, 2, v118
	v_writelane_b32 v242, s43, 44
	v_cmp_gt_i32_e64 s[42:43], v118, v147
	v_bfe_u32 v5, v104, 2, 2
	v_lshlrev_b32_e32 v112, 3, v109
	v_writelane_b32 v243, s42, 31
	v_lshlrev_b32_e32 v7, 2, v107
	v_add_u32_e32 v149, s27, v7
	v_writelane_b32 v243, s43, 32
	v_cmp_lt_i32_e64 s[42:43], v118, v147
	v_add_u32_e32 v151, 0, v7
	v_and_b32_e32 v159, 28, v7
	v_writelane_b32 v243, s42, 33
	v_or_b32_e32 v7, v112, v5
	v_or_b32_e32 v5, v118, v5
	v_writelane_b32 v243, s43, 34
	v_cmp_gt_i32_e64 s[42:43], v8, v147
	v_or_b32_e32 v8, 3, v118
	s_cmpk_lt_i32 s41, 0xe00
	v_writelane_b32 v243, s42, 35
	v_mad_u32_u24 v160, v5, s3, v3
	v_mul_u32_u24_e32 v5, 0x110, v7
	v_writelane_b32 v243, s43, 36
	v_cmp_gt_i32_e64 s[42:43], v8, v147
	v_or_b32_e32 v8, 16, v118
	v_add3_u32 v164, s29, v108, v5
	v_writelane_b32 v243, s42, 37
	s_cselect_b32 s29, s40, s37
	s_mov_b32 s37, 0xe00000
	v_writelane_b32 v243, s43, 38
	v_cmp_gt_i32_e64 s[42:43], v8, v147
	v_or_b32_e32 v8, 17, v118
	v_mad_u32_u24 v165, v7, s3, v3
	v_writelane_b32 v243, s42, 39
	s_movk_i32 s3, 0x400
	s_cselect_b32 s35, s38, s35
	v_writelane_b32 v243, s43, 40
	v_cmp_gt_i32_e64 s[42:43], v8, v147
	v_or_b32_e32 v8, 18, v118
	s_cselect_b32 s37, s37, 0x700000
	v_writelane_b32 v243, s42, 41
	s_cselect_b32 s3, s3, 0xe00
	s_cselect_b32 s36, s39, s36
	v_writelane_b32 v243, s43, 42
	v_cmp_gt_i32_e64 s[42:43], v8, v147
	v_or_b32_e32 v8, 19, v118
	s_mul_hi_i32 s38, s37, s34
	v_writelane_b32 v243, s42, 43
	s_mul_i32 s37, s37, s34
	s_add_u32 s34, s51, s35
	v_writelane_b32 v243, s43, 44
	v_cmp_gt_i32_e64 s[42:43], v8, v147
	v_or_b32_e32 v8, 32, v118
	s_addc_u32 s35, s52, 0
	v_writelane_b32 v243, s42, 45
	s_add_u32 s39, s34, s37
	s_addc_u32 s38, s35, s38
	v_writelane_b32 v243, s43, 46
	v_cmp_gt_i32_e64 s[42:43], v8, v147
	v_or_b32_e32 v8, 33, v118
	s_ashr_i32 s37, s36, 31
	v_writelane_b32 v243, s42, 47
	s_lshl_b64 s[34:35], s[36:37], 1
	v_mov_b32_e32 v111, 0
	v_writelane_b32 v243, s43, 48
	v_cmp_gt_i32_e64 s[42:43], v8, v147
	v_or_b32_e32 v8, 34, v118
	v_and_b32_e32 v110, 48, v104
	v_writelane_b32 v243, s42, 49
	s_add_u32 s34, s39, s34
	v_lshlrev_b32_e32 v4, 3, v1
	v_writelane_b32 v243, s43, 50
	v_cmp_gt_i32_e64 s[42:43], v8, v147
	v_or_b32_e32 v8, 35, v118
	v_or_b32_e32 v156, 8, v154
	v_writelane_b32 v243, s42, 51
	v_lshl_add_u64 v[116:117], s[46:47], 0, v[110:111]
	v_add_u32_e32 v6, 0, v110
	v_writelane_b32 v243, s43, 52
	v_cmp_gt_i32_e64 s[42:43], v8, v147
	v_or_b32_e32 v8, 48, v118
	s_addc_u32 s35, s38, s35
	v_writelane_b32 v243, s42, 53
	v_lshlrev_b32_e32 v110, 4, v1
	v_or_b32_e32 v1, s29, v154
	v_writelane_b32 v243, s43, 54
	v_cmp_gt_i32_e64 s[42:43], v8, v147
	v_or_b32_e32 v8, 49, v118
	v_or_b32_e32 v157, 16, v154
	v_writelane_b32 v243, s42, 55
	v_or_b32_e32 v158, 24, v154
	s_lshr_b32 s2, s2, 1
	v_writelane_b32 v243, s43, 56
	v_cmp_gt_i32_e64 s[42:43], v8, v147
	v_or_b32_e32 v8, 50, v118
	v_lshlrev_b32_e32 v172, 2, v104
	v_writelane_b32 v243, s42, 57
	v_add_u32_e32 v3, 0, v172
	v_add_u32_e32 v3, 0x12b00, v3
	v_writelane_b32 v243, s43, 58
	v_cmp_gt_i32_e64 s[42:43], v8, v147
	v_or_b32_e32 v8, 51, v118
	s_lshl_b32 s41, s44, 4
	v_writelane_b32 v243, s42, 59
	v_and_b32_e32 v13, 0x7f, v104
	v_mul_u32_u24_e32 v14, 0x110, v113
	v_writelane_b32 v243, s43, 60
	v_cmp_gt_i32_e64 s[42:43], v8, v147
	v_or_b32_e32 v8, 64, v118
	v_or_b32_e32 v128, 0xffffff00, v13
	v_writelane_b32 v243, s42, 61
	v_mov_b32_e32 v115, v111
	v_mbcnt_hi_u32_b32 v180, -1, v212
	v_writelane_b32 v243, s43, 62
	v_cmp_gt_i32_e64 s[42:43], v8, v147
	v_or_b32_e32 v8, 0x41, v118
	s_movk_i32 s49, 0x100
	v_writelane_b32 v243, s42, 63
	v_writelane_b32 v243, s30, 14
	s_mov_b32 s55, s31
	v_writelane_b32 v242, s43, 0
	v_cmp_gt_i32_e64 s[42:43], v8, v147
	v_or_b32_e32 v8, 0x42, v118
	v_writelane_b32 v243, s31, 15
	v_writelane_b32 v242, s42, 1
	v_writelane_b32 v243, s44, 29
	v_sub_u32_e32 v129, 0xff, v119
	v_writelane_b32 v242, s43, 2
	v_cmp_gt_i32_e64 s[42:43], v8, v147
	v_or_b32_e32 v8, 0x43, v118
	v_sub_u32_e32 v148, 0xff, v147
	v_writelane_b32 v242, s42, 3
	v_add_u32_e32 v150, 0x100, v149
	v_cmp_lt_u32_e64 s[8:9], 15, v107
	v_writelane_b32 v242, s43, 4
	v_cmp_gt_i32_e64 s[42:43], v8, v147
	v_or_b32_e32 v8, 0x50, v118
	v_cmp_eq_u32_e64 s[10:11], 0, v107
	v_writelane_b32 v242, s42, 5
	v_add_u32_e32 v153, 0xffffff00, v147
	v_add_u32_e32 v161, 0xe00, v160
	v_writelane_b32 v242, s43, 6
	v_cmp_gt_i32_e64 s[42:43], v8, v147
	v_or_b32_e32 v8, 0x51, v118
	v_cmp_gt_i32_e64 s[56:57], v8, v147
	v_or_b32_e32 v8, 0x52, v118
	v_cmp_gt_i32_e64 s[58:59], v8, v147
	v_or_b32_e32 v8, 0x53, v118
	v_cmp_gt_i32_e64 s[60:61], v8, v147
	v_or_b32_e32 v8, 0x60, v118
	v_cmp_gt_i32_e64 s[62:63], v8, v147
	v_or_b32_e32 v8, 0x61, v118
	v_cmp_gt_i32_e64 s[64:65], v8, v147
	v_or_b32_e32 v8, 0x62, v118
	v_cmp_gt_i32_e64 s[66:67], v8, v147
	v_or_b32_e32 v8, 0x63, v118
	v_cmp_gt_i32_e64 s[68:69], v8, v147
	v_or_b32_e32 v8, 0x70, v118
	v_cmp_gt_i32_e64 s[70:71], v8, v147
	v_or_b32_e32 v8, 0x71, v118
	v_cmp_gt_i32_e64 s[72:73], v8, v147
	v_or_b32_e32 v8, 0x72, v118
	v_cmp_gt_i32_e64 s[74:75], v8, v147
	v_or_b32_e32 v8, 0x73, v118
	v_writelane_b32 v242, s42, 11
	v_cmp_gt_i32_e64 s[76:77], v8, v147
	v_lshl_add_u64 v[8:9], s[34:35], 0, v[110:111]
	v_mad_i64_i32 v[10:11], s[34:35], s3, v1, 0
	v_or_b32_e32 v1, s29, v156
	v_writelane_b32 v242, s43, 12
	v_lshl_add_u64 v[120:121], v[10:11], 1, v[8:9]
	v_mad_i64_i32 v[10:11], s[34:35], s3, v1, 0
	v_or_b32_e32 v1, s29, v157
	v_writelane_b32 v242, s51, 9
	v_lshl_add_u64 v[122:123], v[10:11], 1, v[8:9]
	v_mad_i64_i32 v[10:11], s[34:35], s3, v1, 0
	v_or_b32_e32 v1, s29, v158
	v_writelane_b32 v242, s52, 30
	v_lshl_add_u64 v[124:125], v[10:11], 1, v[8:9]
	v_mad_i64_i32 v[10:11], s[34:35], s3, v1, 0
	s_lshl_b32 s3, s45, 5
	v_max_i32_e32 v1, 0x700, v104
	v_writelane_b32 v242, s45, 19
	s_and_b32 s3, s3, 0x3e0
	v_sub_u32_e32 v1, v1, v104
	v_writelane_b32 v242, s3, 36
	v_add_u32_e32 v1, 0x1ff, v1
	v_writelane_b32 v242, s54, 39
	s_and_b32 s3, s28, 3
	v_lshrrev_b32_e32 v5, 9, v1
	v_writelane_b32 v242, s55, 40
	s_lshl_b32 s2, s2, s3
	v_add_u32_e32 v7, 1, v5
	v_add_u32_e32 v5, -1, v5
	v_lshl_add_u64 v[126:127], v[10:11], 1, v[8:9]
	v_writelane_b32 v242, s2, 33
	v_lshlrev_b32_e32 v9, 2, v1
	v_cmp_lt_u32_e64 s[28:29], 1, v5
	v_lshrrev_b32_e32 v8, 1, v5
	s_movk_i32 s2, 0xdff
	v_and_b32_e32 v9, 0xfffff800, v9
	v_writelane_b32 v242, s28, 53
	v_and_b32_e32 v5, 2, v5
	v_cmp_lt_u32_e32 vcc, s2, v1
	v_cmp_gt_u32_e64 s[2:3], 2.0, v1
	v_add_u32_e32 v1, v3, v9
	v_writelane_b32 v242, s29, 54
	v_cmp_eq_u32_e64 s[28:29], 0, v5
	v_cmp_ge_u32_e64 s[78:79], v1, v3
	v_and_b32_e32 v3, 0xfffffe, v7
	v_writelane_b32 v242, s28, 55
	s_and_b64 s[2:3], s[78:79], s[2:3]
	s_and_b64 s[2:3], vcc, s[2:3]
	v_writelane_b32 v242, s29, 56
	v_cmp_ne_u32_e64 s[28:29], v7, v3
	v_lshl_add_u32 v173, v3, 9, v104
	v_lshl_add_u32 v3, v104, 4, 0
	v_writelane_b32 v242, s28, 57
	v_add_u32_e32 v8, 1, v8
	v_add_u32_e32 v175, 0xc000, v3
	v_writelane_b32 v242, s29, 58
	v_writelane_b32 v242, s2, 49
	v_bfrev_b32_e32 v7, 0.5
	v_add_u32_e32 v162, 0x1c00, v160
	v_writelane_b32 v242, s3, 50
	v_writelane_b32 v242, s46, 25
	s_sub_i32 s2, 0, s41
	s_lshl_b32 s3, s26, 1
	v_writelane_b32 v242, s47, 26
	v_writelane_b32 v242, s2, 23
	s_lshl_b32 s2, s50, 4
	s_add_i32 s2, s2, s3
	s_add_i32 s2, s2, 0x80007400
	v_writelane_b32 v242, s2, 51
	s_add_i32 s2, 0, 0x25de0
	v_writelane_b32 v242, s2, 21
	s_add_i32 s2, 0, 0x25db8
	v_writelane_b32 v243, s2, 19
	s_add_i32 s2, 0, 0x25dd0
	v_writelane_b32 v243, s2, 20
	s_add_i32 s2, 0, 0x25da8
	v_writelane_b32 v242, s2, 10
	s_add_i32 s2, 0, 0x25dd8
	v_writelane_b32 v243, s2, 21
	s_add_i32 s2, 0, 0x25db0
	v_writelane_b32 v243, s2, 23
	s_add_i32 s2, s48, 0x820
	v_writelane_b32 v242, s2, 34
	s_add_i32 s2, s48, 0xc30
	v_writelane_b32 v242, s2, 35
	s_add_i32 s2, s48, 0x1040
	v_writelane_b32 v242, s2, 38
	s_add_i32 s2, s48, 0x1450
	v_writelane_b32 v242, s2, 24
	s_add_i32 s2, s48, 0x1860
	v_writelane_b32 v242, s2, 27
	v_add_u32_e32 v163, 0x2a00, v160
	v_add_u32_e32 v166, 0x2200, v164
	v_add_u32_e32 v167, 0xe00, v165
	v_add_u32_e32 v168, 0x4400, v164
	v_add_u32_e32 v169, 0x1c00, v165
	v_add_u32_e32 v170, 0x6600, v164
	v_add_u32_e32 v171, 0x2a00, v165
	v_mov_b32_e32 v1, v128
	v_add_u32_e32 v105, 0x200, v104
	v_and_b32_e32 v174, -2, v8
	v_lshl_add_u64 v[130:131], s[46:47], 0, v[114:115]
	v_add_u32_e32 v115, 0xfffffe00, v104
	v_add_u32_e32 v176, s27, v172
	s_sub_i32 s40, 0, s33
	v_add_u32_e32 v177, 0x10900, v151
	v_sub_u32_e32 v178, 0, v119
	v_lshlrev_b32_e32 v132, 1, v112
	s_mov_b32 s42, 0x3f2aaaab
	v_mov_b32_e32 v179, 0x3ecc95a3
	s_mov_b32 s43, 0x3f317218
	s_mov_b32 s44, 0x7f800000
	s_mov_b32 s45, 0x33800000
	v_lshlrev_b32_e32 v134, 2, v118
	v_add_u32_e32 v181, v2, v114
	s_xor_b64 s[26:27], s[6:7], -1
	v_lshlrev_b32_e32 v110, 1, v4
	v_writelane_b32 v242, s48, 7
	s_add_i32 s2, s48, 0x1c70
	v_add_u32_e32 v182, v12, v14
	v_mov_b32_e32 v2, v111
	v_mov_b32_e32 v3, v111
	v_mov_b32_e32 v4, v111
	v_mov_b32_e32 v5, v111
	v_mov_b32_e32 v136, 0x3f317218
	v_mov_b32_e32 v183, 0x7f800000
	v_mov_b32_e32 v184, 0x7fc00000
	v_mov_b32_e32 v185, 0xff800000
	v_lshl_or_b32 v186, v180, 2, v7
	v_add_u32_e32 v187, v6, v14
	v_mov_b32_e32 v188, 0x7c
	v_writelane_b32 v242, s2, 29
	s_branch .LBB0_4992
